# speedup vs baseline: 1.0091x; 1.0091x over previous
.LBB0_36:
	s_endpgm
	.p2align	8

_Z14attn_bh_kernelPKDF16_S0_S0_PDF16_i:
	s_load_dwordx4 s[8:11], s[0:1], 0x0
	s_load_dwordx2 s[4:5], s[0:1], 0x10
	s_load_dword s3, s[0:1], 0x20
	v_lshrrev_b32_e32 v2, 6, v0
	v_and_b32_e32 v86, 31, v0
	s_lshr_b32 s6, s2, 3
	s_mul_i32 s12, s6, 0x248
	s_waitcnt lgkmcnt(0)
	v_add_u32_e32 v87, s3, v2
	v_lshl_or_b32 v2, v87, 5, v86
	v_min_i32_e32 v2, 0x247, v2
	v_add_u32_e32 v2, s12, v2
	v_ashrrev_i32_e32 v3, 31, v2
	s_lshl_b32 s3, s2, 6
	v_lshlrev_b64 v[2:3], 10, v[2:3]
	s_and_b32 s14, s3, 0x1c0
	v_bfe_u32 v1, v0, 5, 1
	v_lshl_add_u64 v[2:3], s[8:9], 0, v[2:3]
	s_mov_b32 s7, 0
	s_lshl_b32 s6, s14, 1
	v_mov_b32_e32 v45, 0
	v_lshl_add_u64 v[2:3], v[2:3], 0, s[6:7]
	v_lshlrev_b32_e32 v42, 4, v1
	v_mov_b32_e32 v43, v45
	s_mul_hi_i32 s3, s2, 0x12400
	s_mul_i32 s2, s2, 0x12400
	v_lshl_add_u64 v[2:3], v[2:3], 0, v[42:43]
	s_add_u32 s2, s4, s2
	global_load_dwordx4 v[66:69], v[2:3], off
	global_load_dwordx4 v[70:73], v[2:3], off offset:32
	global_load_dwordx4 v[74:77], v[2:3], off offset:64
	global_load_dwordx4 v[78:81], v[2:3], off offset:96
	s_addc_u32 s3, s5, s3
	s_ashr_i32 s13, s12, 31
	s_lshl_b64 s[16:17], s[12:13], 10
	s_add_u32 s16, s10, s16
	s_addc_u32 s17, s11, s17
	s_add_u32 s16, s16, s6
	s_addc_u32 s17, s17, 0
	v_lshrrev_b32_e32 v4, 6, v0
	v_and_b32_e32 v5, 63, v0
	v_lshrrev_b32_e32 v6, 3, v5
	v_readfirstlane_b32 s15, v4
	v_and_b32_e32 v7, 7, v5
	s_movk_i32 s23, 0x400
	s_movk_i32 s24, 0x490
	s_mov_b32 s19, 0x10000
	s_movk_i32 s20, 0x80
	s_and_b32 s18, s15, 7
	s_lshl_b32 s21, s18, 3
	s_lshl_b32 s18, s18, 10
	v_add_u32_e32 v9, s21, v6
	s_cmp_lt_u32 s15, 8
	s_cselect_b32 s23, s23, s24
	s_cselect_b32 s21, s19, s20
	s_cselect_b32 s16, s16, s2
	s_cselect_b32 s17, s17, s3
	s_cselect_b32 s24, 0, 0x12400
	s_add_u32 s18, s18, s24
	v_bfe_u32 v10, v9, 1, 3
	v_xor_b32_e32 v10, v10, v7
	v_mul_u32_u24_e32 v8, s23, v9
	v_lshl_add_u32 v8, v10, 4, v8
	s_mov_b32 m0, s18
	s_add_u32 s18, s18, 0x2000
	global_load_lds_dwordx4 v8, s[16:17]
	v_add_u32_e32 v8, s21, v8
	s_mov_b32 m0, s18
	s_add_u32 s18, s18, 0x2000
	global_load_lds_dwordx4 v8, s[16:17]
	v_add_u32_e32 v8, s21, v8
	s_mov_b32 m0, s18
	s_add_u32 s18, s18, 0x2000
	global_load_lds_dwordx4 v8, s[16:17]
	v_add_u32_e32 v8, s21, v8
	s_cmp_lg_u32 s15, 0
	s_cbranch_scc1 .Lat_nw0
	v_add_u32_e32 v11, 0x60000, v8
	s_mov_b32 m0, 0x12000
	s_nop 0
	global_load_lds_dwordx4 v11, s[16:17]
.Lat_nw0:
	s_cmp_lg_u32 s15, 8
	s_cbranch_scc1 .Lat_nw8
	v_mul_u32_u24_e32 v11, 0x490, v5
	global_load_dwordx4 v[12:15], v11, s[16:17] offset:1152
.Lat_nw8:
	s_waitcnt vmcnt(0)
	s_cmp_lt_u32 s15, 8
	s_cbranch_scc1 .Lat_nt9
	s_sub_u32 s24, s15, 8
	v_bfe_u32 v16, v5, 1, 3
	v_xor_b32_e32 v16, s24, v16
	v_lshlrev_b32_e32 v17, 7, v5
	v_lshl_add_u32 v16, v16, 4, v17
	v_add_u32_e32 v16, 0x24400, v16
	s_cmp_eq_u32 s15, 8
	s_cbranch_scc1 .Lat_t9d
	v_mov_b32_e32 v12, 0
	v_mov_b32_e32 v13, 0
	v_mov_b32_e32 v14, 0
	v_mov_b32_e32 v15, 0
.Lat_t9d:
	ds_write_b128 v16, v[12:15]
.Lat_nt9:
	v_and_b32_e32 v2, 19, v0
	v_lshlrev_b32_e32 v3, 1, v0
	v_lshrrev_b32_e32 v0, 1, v0
	v_and_b32_e32 v3, 8, v3
	v_and_b32_e32 v0, 4, v0
	v_or3_b32 v0, v3, v2, v0
	v_lshrrev_b32_e32 v2, 1, v0
	v_bfe_u32 v3, v0, 1, 3
	v_lshlrev_b32_e32 v0, 7, v0
	v_bitop3_b32 v2, v1, v2, 7 bitop3:0x78
	v_lshl_add_u32 v88, v2, 4, v0
	v_bitop3_b32 v2, v1, v3, 2 bitop3:0x36
	v_lshl_add_u32 v89, v2, 4, v0
	v_bitop3_b32 v2, v1, v3, 4 bitop3:0x36
	v_lshl_add_u32 v90, v2, 4, v0
	v_bitop3_b32 v2, v1, v3, 6 bitop3:0x36
	v_lshl_add_u32 v91, v2, 4, v0
	v_bfe_u32 v3, v86, 1, 3
	v_lshlrev_b32_e32 v2, 7, v86
	v_add_u32_e32 v2, 0x12400, v2
	v_xor_b32_e32 v4, v1, v3
	v_lshl_add_u32 v93, v4, 4, v2
	v_or_b32_e32 v4, 2, v1
	v_xor_b32_e32 v4, v4, v3
	v_lshl_add_u32 v114, v4, 4, v2
	v_or_b32_e32 v4, 4, v1
	v_xor_b32_e32 v4, v4, v3
	v_lshl_add_u32 v115, v4, 4, v2
	v_or_b32_e32 v4, 6, v1
	v_xor_b32_e32 v4, v4, v3
	v_lshl_add_u32 v116, v4, 4, v2
	s_mov_b32 s22, 1
	v_cmp_gt_i32_e32 vcc, 19, v87
	s_waitcnt lgkmcnt(0)
	s_barrier
	s_mov_b32 m0, s18
	s_add_u32 s18, s18, 0x2000
	global_load_lds_dwordx4 v8, s[16:17]
	v_add_u32_e32 v8, s21, v8
	s_mov_b32 m0, s18
	s_add_u32 s18, s18, 0x2000
	global_load_lds_dwordx4 v8, s[16:17]
	v_add_u32_e32 v8, s21, v8
	s_mov_b32 m0, s18
	s_add_u32 s18, s18, 0x2000
	global_load_lds_dwordx4 v8, s[16:17]
	v_add_u32_e32 v8, s21, v8
	s_mov_b32 m0, s18
	s_add_u32 s18, s18, 0x2000
	global_load_lds_dwordx4 v8, s[16:17]
	v_add_u32_e32 v8, s21, v8
	s_mov_b32 m0, s18
	s_add_u32 s18, s18, 0x2000
	global_load_lds_dwordx4 v8, s[16:17]
	v_add_u32_e32 v8, s21, v8
	s_mov_b32 m0, s18
	s_add_u32 s18, s18, 0x2000
	global_load_lds_dwordx4 v8, s[16:17]
	v_add_u32_e32 v8, s21, v8
	s_and_saveexec_b64 s[2:3], vcc
	s_cbranch_execz .Lat_notile
	s_load_dwordx2 s[4:5], s[0:1], 0x18
	v_lshlrev_b32_e32 v92, 3, v1
	s_add_u32 s0, s8, s6
	v_mov_b32_e32 v0, 0
	s_addc_u32 s1, s9, 0
	v_lshlrev_b32_e32 v2, 1, v92
	v_mov_b32_e32 v3, v0
	v_or_b32_e32 v1, s14, v92
	v_lshl_add_u64 v[82:83], s[0:1], 0, v[2:3]
	s_mov_b32 s7, 0x20000
	s_brev_b32 s6, -2
	s_waitcnt lgkmcnt(0)
	s_and_b32 s5, s5, 0xffff
	s_mov_b64 s[2:3], 0
	s_movk_i32 s13, 0x248
	v_mov_b32_e32 v94, 0x247
	s_movk_i32 s18, 0x205
	s_mov_b32 s19, 0x41000000
	s_mov_b32 s20, 0xc1000000
	v_lshlrev_b32_e32 v95, 1, v1
	v_mov_b32_e32 v96, 0xf149f2ca
	v_mov_b32_e32 v97, v87
	s_branch .LBB2_9

.LBB2_11:
	s_or_b64 exec, exec, s[8:9]
	v_or_b32_e32 v1, 31, v1
	v_min_i32_e32 v2, 0x247, v1
	v_add_u32_e32 v2, 64, v2
	v_ashrrev_i32_e32 v2, 6, v2
	v_cmp_lt_i32_e32 vcc, s18, v1
	v_mov_b32_e32 v17, 0
	v_mov_b32_e32 v35, 0
	v_cndmask_b32_e32 v85, 9, v2, vcc
	v_cmp_lt_i32_e32 vcc, 0, v85
	v_mov_b32_e32 v34, 0
	v_mov_b32_e32 v14, 0
	v_mov_b32_e32 v13, 0
	v_mov_b32_e32 v37, 0
	v_mov_b32_e32 v36, 0
	v_mov_b32_e32 v10, 0
	v_mov_b32_e32 v9, 0
	v_mov_b32_e32 v39, 0
	v_mov_b32_e32 v38, 0
	v_mov_b32_e32 v6, 0
	v_mov_b32_e32 v5, 0
	v_mov_b32_e32 v41, 0
	v_mov_b32_e32 v40, 0
	v_mov_b32_e32 v2, 0
	v_mov_b32_e32 v33, 0
	v_mov_b32_e32 v43, 0
	v_mov_b32_e32 v42, 0
	v_mov_b32_e32 v30, 0
	v_mov_b32_e32 v29, 0
	v_mov_b32_e32 v45, 0
	v_mov_b32_e32 v44, 0
	v_mov_b32_e32 v26, 0
	v_mov_b32_e32 v25, 0
	v_mov_b32_e32 v47, 0
	v_mov_b32_e32 v46, 0
	v_mov_b32_e32 v22, 0
	v_mov_b32_e32 v21, 0
	v_mov_b32_e32 v49, 0
	v_mov_b32_e32 v48, 0
	v_mov_b32_e32 v18, 0
	v_mov_b32_e32 v1, 0
	s_and_saveexec_b64 s[8:9], vcc
	s_cbranch_execz .LBB2_23
	v_mov_b32_e32 v14, v0
	v_mov_b32_e32 v15, v0
	v_max_i32_e32 v98, 0x205, v3
	v_mov_b32_e32 v1, v0
	v_mov_b32_e32 v2, v0
	v_mov_b32_e32 v3, v0
	v_mov_b32_e32 v4, v0
	v_mov_b32_e32 v5, v0
	v_mov_b32_e32 v6, v0
	v_mov_b32_e32 v7, v0
	v_mov_b32_e32 v8, v0
	v_mov_b32_e32 v9, v0
	v_mov_b32_e32 v10, v0
	v_mov_b32_e32 v11, v0
	v_mov_b32_e32 v12, v0
	v_mov_b32_e32 v13, v0
	v_mov_b64_e32 v[32:33], v[14:15]
	v_mov_b64_e32 v[30:31], v[12:13]
	v_mov_b64_e32 v[28:29], v[10:11]
	v_mov_b64_e32 v[26:27], v[8:9]
	v_mov_b64_e32 v[24:25], v[6:7]
	v_mov_b64_e32 v[22:23], v[4:5]
	v_mov_b64_e32 v[20:21], v[2:3]
	v_mov_b64_e32 v[18:19], v[0:1]
	v_mov_b64_e32 v[16:17], v[14:15]
	s_mov_b32 s21, 0
	v_mov_b32_e32 v104, 0
	s_mov_b64 s[10:11], 0
	v_mov_b64_e32 v[14:15], v[12:13]
	v_mov_b64_e32 v[12:13], v[10:11]
	v_mov_b64_e32 v[10:11], v[8:9]
	v_mov_b64_e32 v[8:9], v[6:7]
	v_mov_b64_e32 v[6:7], v[4:5]
	v_mov_b64_e32 v[4:5], v[2:3]
	v_mov_b64_e32 v[2:3], v[0:1]
	v_mov_b32_e32 v1, 0
	v_mov_b32_e32 v99, v88
	v_mov_b32_e32 v100, v89
	v_mov_b32_e32 v101, v90
	v_mov_b32_e32 v102, v91
	v_mov_b32_e32 v103, v93
	v_mov_b32_e32 v117, v114
	v_mov_b32_e32 v118, v115
	v_mov_b32_e32 v119, v116
	s_branch .LBB2_14
.LBB2_13:
	v_exp_f32_e32 v105, v50
	v_exp_f32_e32 v106, v51
	v_exp_f32_e32 v107, v52
	v_exp_f32_e32 v108, v53
	ds_read_b128 v[50:53], v103
	v_exp_f32_e32 v109, v54
	v_exp_f32_e32 v110, v55
	v_exp_f32_e32 v111, v56
	v_exp_f32_e32 v57, v57
	v_cvt_pkrtz_f16_f32 v54, v105, v106
	v_cvt_pkrtz_f16_f32 v55, v107, v108
	v_cvt_pkrtz_f16_f32 v56, v109, v110
	v_cvt_pkrtz_f16_f32 v57, v111, v57
	ds_read_b128 v[106:109], v117
	v_exp_f32_e32 v105, v58
	s_waitcnt lgkmcnt(1)
	v_mfma_f32_32x32x16_f16 v[18:33], v[50:53], v[54:57], v[18:33]
	ds_read_b128 v[50:53], v103 offset:4096
	v_exp_f32_e32 v110, v59
	v_exp_f32_e32 v111, v60
	v_exp_f32_e32 v112, v61
	ds_read_b128 v[58:61], v117 offset:4096
	v_exp_f32_e32 v62, v62
	v_exp_f32_e32 v41, v41
	s_waitcnt lgkmcnt(1)
	v_mfma_f32_32x32x16_f16 v[2:17], v[50:53], v[54:57], v[2:17]
	v_exp_f32_e32 v52, v63
	v_exp_f32_e32 v53, v64
	v_exp_f32_e32 v63, v65
	v_cvt_pkrtz_f16_f32 v50, v105, v110
	v_cvt_pkrtz_f16_f32 v51, v111, v112
	v_cvt_pkrtz_f16_f32 v52, v62, v52
	v_cvt_pkrtz_f16_f32 v53, v53, v63
	v_exp_f32_e32 v62, v34
	v_exp_f32_e32 v63, v35
	v_exp_f32_e32 v64, v36
	v_exp_f32_e32 v65, v37
	ds_read_b128 v[34:37], v118
	v_mfma_f32_32x32x16_f16 v[18:33], v[106:109], v[50:53], v[18:33]
	v_exp_f32_e32 v105, v38
	v_exp_f32_e32 v106, v39
	v_cvt_pkrtz_f16_f32 v38, v62, v63
	v_cvt_pkrtz_f16_f32 v39, v64, v65
	v_exp_f32_e32 v62, v42
	v_exp_f32_e32 v63, v43
	v_exp_f32_e32 v64, v44
	s_waitcnt lgkmcnt(1)
	v_mfma_f32_32x32x16_f16 v[2:17], v[58:61], v[50:53], v[2:17]
	v_exp_f32_e32 v58, v40
	v_cvt_pkrtz_f16_f32 v40, v105, v106
	v_exp_f32_e32 v65, v45
	ds_read_b128 v[42:45], v119 offset:4096
	v_cvt_pkrtz_f16_f32 v41, v58, v41
	ds_read_b128 v[58:61], v119
	v_exp_f32_e32 v46, v46
	s_waitcnt lgkmcnt(2)
	v_mfma_f32_32x32x16_f16 v[18:33], v[34:37], v[38:41], v[18:33]
	ds_read_b128 v[34:37], v118 offset:4096
	v_add_u32_e32 v85, -1, v85
	s_add_i32 s21, s21, 64
	v_cmp_eq_u32_e32 vcc, 0, v85
	v_add_u32_e32 v99, 0x2000, v99
	v_add_u32_e32 v100, 0x2000, v100
	v_add_u32_e32 v101, 0x2000, v101
	s_waitcnt lgkmcnt(0)
	v_mfma_f32_32x32x16_f16 v[2:17], v[34:37], v[38:41], v[2:17]
	v_exp_f32_e32 v36, v47
	v_exp_f32_e32 v37, v48
	v_exp_f32_e32 v47, v49
	v_cvt_pkrtz_f16_f32 v34, v62, v63
	v_cvt_pkrtz_f16_f32 v35, v64, v65
	v_cvt_pkrtz_f16_f32 v36, v46, v36
	v_cvt_pkrtz_f16_f32 v37, v37, v47
	v_pk_add_f16 v46, v55, v51
	v_pk_add_f16 v47, v57, v53
	v_pk_add_f16 v48, v54, v50
	v_pk_add_f16 v49, v56, v52
	v_pk_add_f16 v39, v39, v35
	v_pk_add_f16 v41, v41, v37
	v_pk_add_f16 v38, v38, v34
	v_pk_add_f16 v40, v40, v36
	v_pk_add_f16 v38, v38, v48
	v_pk_add_f16 v40, v40, v49
	v_pk_add_f16 v41, v41, v47
	v_pk_add_f16 v39, v39, v46
	v_mfma_f32_32x32x16_f16 v[18:33], v[58:61], v[34:37], v[18:33]
	v_pk_add_f16 v39, v39, v41
	v_pk_add_f16 v38, v38, v40
	v_cvt_f32_f16_e32 v41, v39
	v_cvt_f32_f16_e32 v40, v38
	v_cvt_f32_f16_sdwa v39, v39 dst_sel:DWORD dst_unused:UNUSED_PAD src0_sel:WORD_1
	v_cvt_f32_f16_sdwa v38, v38 dst_sel:DWORD dst_unused:UNUSED_PAD src0_sel:WORD_1
	v_add_u32_e32 v102, 0x2000, v102
	v_mfma_f32_32x32x16_f16 v[2:17], v[42:45], v[34:37], v[2:17]
	v_add_f32_e32 v34, v39, v41
	v_add_f32_e32 v35, v38, v40
	v_add_f32_e32 v34, v35, v34
	v_add_f32_e32 v1, v1, v34
	s_or_b64 s[10:11], vcc, s[10:11]
	v_add_u32_e32 v103, 0x2000, v103
	v_add_u32_e32 v117, 0x2000, v117
	v_add_u32_e32 v118, 0x2000, v118
	v_add_u32_e32 v119, 0x2000, v119
	s_andn2_b64 exec, exec, s[10:11]
	s_cbranch_execz .LBB2_22
.LBB2_14:
	s_cmp_eq_u32 s22, 0
	s_cbranch_scc1 .Lat_qkA
	s_cmp_lg_u32 s21, 0xc0
	s_cbranch_scc1 .Lat_qkB
	s_waitcnt vmcnt(0)
	s_barrier
	s_mov_b32 s22, 0
	s_branch .Lat_qkA
.Lat_qkB:
	ds_read_b128 v[34:37], v99
	ds_read_b128 v[38:41], v99 offset:4096
	ds_read_b128 v[106:109], v100
	ds_read_b128 v[110:113], v100 offset:4096
	s_cmpk_gt_u32 s21, 0x1c6
	s_waitcnt lgkmcnt(3)
	v_mfma_f32_32x32x16_f16 v[50:65], v[34:37], v[66:69], 0
	s_waitcnt lgkmcnt(2)
	v_mfma_f32_32x32x16_f16 v[34:49], v[38:41], v[66:69], 0
	s_waitcnt lgkmcnt(1)
	v_mfma_f32_32x32x16_f16 v[50:65], v[106:109], v[70:73], v[50:65]
	s_waitcnt lgkmcnt(0)
	v_mfma_f32_32x32x16_f16 v[34:49], v[110:113], v[70:73], v[34:49]
	ds_read_b128 v[106:109], v101
	ds_read_b128 v[110:113], v101 offset:4096
	s_waitcnt lgkmcnt(1)
	v_mfma_f32_32x32x16_f16 v[50:65], v[106:109], v[74:77], v[50:65]
	s_waitcnt lgkmcnt(0)
	v_mfma_f32_32x32x16_f16 v[34:49], v[110:113], v[74:77], v[34:49]
	ds_read_b128 v[106:109], v102
	ds_read_b128 v[110:113], v102 offset:4096
	s_waitcnt lgkmcnt(1)
	v_mfma_f32_32x32x16_f16 v[50:65], v[106:109], v[78:81], v[50:65]
	s_waitcnt lgkmcnt(0)
	v_mfma_f32_32x32x16_f16 v[34:49], v[110:113], v[78:81], v[34:49]
	s_branch .Lat_qkJ

.Lat_qkJ:
	s_cbranch_scc0 .LBB2_16
	v_add_u32_e32 v105, s21, v92
	v_cmp_le_u32_e32 vcc, v105, v98
	v_add_u32_e32 v106, 32, v105
	s_nop 5
	v_cndmask_b32_e32 v50, v96, v50, vcc
	v_cmp_le_u32_e32 vcc, v106, v98
	v_add_u32_e32 v106, 33, v105
	s_nop 0
	v_cndmask_b32_e32 v34, v96, v34, vcc
	v_cmp_lt_u32_e32 vcc, v105, v98
	s_nop 1
	v_cndmask_b32_e32 v51, v96, v51, vcc
	v_cmp_le_u32_e32 vcc, v106, v98
	v_add_u32_e32 v106, 2, v105
	s_nop 0
	v_cndmask_b32_e32 v35, v96, v35, vcc
	v_cmp_le_u32_e32 vcc, v106, v98
	v_add_u32_e32 v106, 34, v105
	s_nop 0
	v_cndmask_b32_e32 v52, v96, v52, vcc
	v_cmp_le_u32_e32 vcc, v106, v98
	v_add_u32_e32 v106, 3, v105
	s_nop 0
	v_cndmask_b32_e32 v36, v96, v36, vcc
	v_cmp_le_u32_e32 vcc, v106, v98
	v_add_u32_e32 v106, 35, v105
	s_nop 0
	v_cndmask_b32_e32 v53, v96, v53, vcc
	v_cmp_le_u32_e32 vcc, v106, v98
	v_add_u32_e32 v106, 4, v105
	s_nop 0
	v_cndmask_b32_e32 v37, v96, v37, vcc
	v_cmp_le_u32_e32 vcc, v106, v98
	v_add_u32_e32 v106, 36, v105
	s_nop 0
	v_cndmask_b32_e32 v54, v96, v54, vcc
	v_cmp_le_u32_e32 vcc, v106, v98
	v_add_u32_e32 v106, 5, v105
	s_nop 0
	v_cndmask_b32_e32 v38, v96, v38, vcc
	v_cmp_le_u32_e32 vcc, v106, v98
	v_add_u32_e32 v106, 37, v105
	s_nop 0
	v_cndmask_b32_e32 v55, v96, v55, vcc
	v_cmp_le_u32_e32 vcc, v106, v98
	v_add_u32_e32 v106, 6, v105
	s_nop 0
	v_cndmask_b32_e32 v39, v96, v39, vcc
	v_cmp_le_u32_e32 vcc, v106, v98
	v_add_u32_e32 v106, 38, v105
	s_nop 0
	v_cndmask_b32_e32 v56, v96, v56, vcc
	v_cmp_le_u32_e32 vcc, v106, v98
	v_add_u32_e32 v106, 7, v105
	s_nop 0
	v_cndmask_b32_e32 v40, v96, v40, vcc
	v_cmp_le_u32_e32 vcc, v106, v98
	v_add_u32_e32 v106, 39, v105
	s_nop 0
	v_cndmask_b32_e32 v57, v96, v57, vcc
	v_cmp_le_u32_e32 vcc, v106, v98
	v_add_u32_e32 v106, 16, v105
	s_nop 0
	v_cndmask_b32_e32 v41, v96, v41, vcc
	v_cmp_le_u32_e32 vcc, v106, v98
	v_add_u32_e32 v106, 48, v105
	s_nop 0
	v_cndmask_b32_e32 v58, v96, v58, vcc
	v_cmp_le_u32_e32 vcc, v106, v98
	v_add_u32_e32 v106, 17, v105
	s_nop 0
	v_cndmask_b32_e32 v42, v96, v42, vcc
	v_cmp_le_u32_e32 vcc, v106, v98
	v_add_u32_e32 v106, 49, v105
	s_nop 0
	v_cndmask_b32_e32 v59, v96, v59, vcc
	v_cmp_le_u32_e32 vcc, v106, v98
	v_add_u32_e32 v106, 18, v105
	s_nop 0
	v_cndmask_b32_e32 v43, v96, v43, vcc
	v_cmp_le_u32_e32 vcc, v106, v98
	v_add_u32_e32 v106, 50, v105
	s_nop 0
	v_cndmask_b32_e32 v60, v96, v60, vcc
	v_cmp_le_u32_e32 vcc, v106, v98
	v_add_u32_e32 v106, 19, v105
	s_nop 0
	v_cndmask_b32_e32 v44, v96, v44, vcc
	v_cmp_le_u32_e32 vcc, v106, v98
	v_add_u32_e32 v106, 51, v105
	s_nop 0
	v_cndmask_b32_e32 v61, v96, v61, vcc
	v_cmp_le_u32_e32 vcc, v106, v98
	v_add_u32_e32 v106, 20, v105
	s_nop 0
	v_cndmask_b32_e32 v45, v96, v45, vcc
	v_cmp_le_u32_e32 vcc, v106, v98
	v_add_u32_e32 v106, 52, v105
	s_nop 0
	v_cndmask_b32_e32 v62, v96, v62, vcc
	v_cmp_le_u32_e32 vcc, v106, v98
	v_add_u32_e32 v106, 21, v105
	s_nop 0
	v_cndmask_b32_e32 v46, v96, v46, vcc
	v_cmp_le_u32_e32 vcc, v106, v98
	v_add_u32_e32 v106, 53, v105
	s_nop 0
	v_cndmask_b32_e32 v63, v96, v63, vcc
	v_cmp_le_u32_e32 vcc, v106, v98
	v_add_u32_e32 v106, 22, v105
	s_nop 0
	v_cndmask_b32_e32 v47, v96, v47, vcc
	v_cmp_le_u32_e32 vcc, v106, v98
	v_add_u32_e32 v106, 54, v105
	s_nop 0
	v_cndmask_b32_e32 v64, v96, v64, vcc
	v_cmp_le_u32_e32 vcc, v106, v98
	v_add_u32_e32 v106, 23, v105
	v_add_u32_e32 v105, 55, v105
	v_cndmask_b32_e32 v48, v96, v48, vcc
	v_cmp_le_u32_e32 vcc, v106, v98
	s_nop 1
	v_cndmask_b32_e32 v65, v96, v65, vcc
	v_cmp_le_u32_e32 vcc, v105, v98
	s_nop 1
	v_cndmask_b32_e32 v49, v96, v49, vcc

.Lat_notile:
	s_waitcnt vmcnt(0)
	s_barrier
	s_endpgm
	.p2align	8

	.amdhsa_kernel _Z14attn_bh_kernelPKDF16_S0_S0_PDF16_i
		.amdhsa_group_segment_fixed_size 0
		.amdhsa_private_segment_fixed_size 0
		.amdhsa_kernarg_size 36
		.amdhsa_user_sgpr_count 2
		.amdhsa_user_sgpr_dispatch_ptr 0
		.amdhsa_user_sgpr_queue_ptr 0
		.amdhsa_user_sgpr_kernarg_segment_ptr 1
		.amdhsa_user_sgpr_dispatch_id 0
		.amdhsa_user_sgpr_kernarg_preload_length 0
		.amdhsa_user_sgpr_kernarg_preload_offset 0
		.amdhsa_user_sgpr_private_segment_size 0
		.amdhsa_uses_dynamic_stack 0
		.amdhsa_enable_private_segment 0
		.amdhsa_system_sgpr_workgroup_id_x 1
		.amdhsa_system_sgpr_workgroup_id_y 0
		.amdhsa_system_sgpr_workgroup_id_z 0
		.amdhsa_system_sgpr_workgroup_info 0
		.amdhsa_system_vgpr_workitem_id 0
		.amdhsa_next_free_vgpr 120
		.amdhsa_next_free_sgpr 25
		.amdhsa_accum_offset 120
		.amdhsa_reserve_vcc 1
		.amdhsa_float_round_mode_32 0
		.amdhsa_float_round_mode_16_64 0
		.amdhsa_float_denorm_mode_32 3
		.amdhsa_float_denorm_mode_16_64 3
		.amdhsa_dx10_clamp 1
		.amdhsa_ieee_mode 1
		.amdhsa_fp16_overflow 0
		.amdhsa_tg_split 0
		.amdhsa_exception_fp_ieee_invalid_op 0
		.amdhsa_exception_fp_denorm_src 0
		.amdhsa_exception_fp_ieee_div_zero 0
		.amdhsa_exception_fp_ieee_overflow 0
		.amdhsa_exception_fp_ieee_underflow 0
		.amdhsa_exception_fp_ieee_inexact 0
		.amdhsa_exception_int_div_zero 0
	.end_amdhsa_kernel

	.text
	.p2alignl 6, 3212836864
	.fill 256, 4, 3212836864
	.p2align	8

amdhsa.kernels:
  - .agpr_count:     0
    .args:
      - .offset:         0
        .size:           136
        .value_kind:     by_value
      - .actual_access:  read_only
        .address_space:  global
        .offset:         136
        .size:           8
        .value_kind:     global_buffer
      - .actual_access:  read_only
        .address_space:  global
        .offset:         144
        .size:           8
        .value_kind:     global_buffer
      - .actual_access:  read_only
        .address_space:  global
        .offset:         152
        .size:           8
        .value_kind:     global_buffer
      - .actual_access:  read_only
        .address_space:  global
        .offset:         160
        .size:           8
        .value_kind:     global_buffer
      - .actual_access:  write_only
        .address_space:  global
        .offset:         168
        .size:           8
        .value_kind:     global_buffer
      - .actual_access:  write_only
        .address_space:  global
        .offset:         176
        .size:           8
        .value_kind:     global_buffer
    .group_segment_fixed_size: 0
    .kernarg_segment_align: 8
    .kernarg_segment_size: 184
    .language:       OpenCL C
    .language_version:
      - 2
      - 0
    .max_flat_workgroup_size: 256
    .name:           _Z15prologue_kernel8PrepArgsPKfS1_PKiS1_PDF16_Pf
    .private_segment_fixed_size: 0
    .sgpr_count:     36
    .sgpr_spill_count: 0
    .symbol:         _Z15prologue_kernel8PrepArgsPKfS1_PKiS1_PDF16_Pf.kd
    .uniform_work_group_size: 1
    .uses_dynamic_stack: false
    .vgpr_count:     44
    .vgpr_spill_count: 0
    .wavefront_size: 64
  - .agpr_count:     0
    .args:
      - .actual_access:  read_only
        .address_space:  global
        .offset:         0
        .size:           8
        .value_kind:     global_buffer
      - .offset:         8
        .size:           4
        .value_kind:     by_value
      - .offset:         12
        .size:           4
        .value_kind:     by_value
      - .actual_access:  read_only
        .address_space:  global
        .offset:         16
        .size:           8
        .value_kind:     global_buffer
      - .actual_access:  read_only
        .address_space:  global
        .offset:         24
        .size:           8
        .value_kind:     global_buffer
      - .actual_access:  read_only
        .address_space:  global
        .offset:         32
        .size:           8
        .value_kind:     global_buffer
      - .actual_access:  read_only
        .address_space:  global
        .offset:         40
        .size:           8
        .value_kind:     global_buffer
      - .address_space:  global
        .offset:         48
        .size:           8
        .value_kind:     global_buffer
      - .actual_access:  write_only
        .address_space:  global
        .offset:         56
        .size:           8
        .value_kind:     global_buffer
    .group_segment_fixed_size: 0
    .kernarg_segment_align: 8
    .kernarg_segment_size: 64
    .language:       OpenCL C
    .language_version:
      - 2
      - 0
    .max_flat_workgroup_size: 256
    .name:           _Z18ffn2_finish_kernelPKfiiS0_PK15HIP_vector_typeIfLj2EES0_S0_PDF16_PS2_
    .private_segment_fixed_size: 0
    .sgpr_count:     20
    .sgpr_spill_count: 0
    .symbol:         _Z18ffn2_finish_kernelPKfiiS0_PK15HIP_vector_typeIfLj2EES0_S0_PDF16_PS2_.kd
    .uniform_work_group_size: 1
    .uses_dynamic_stack: false
    .vgpr_count:     52
    .vgpr_spill_count: 0
    .wavefront_size: 64
  - .agpr_count:     0
    .args:
      - .actual_access:  read_only
        .address_space:  global
        .offset:         0
        .size:           8
        .value_kind:     global_buffer
      - .actual_access:  read_only
        .address_space:  global
        .offset:         8
        .size:           8
        .value_kind:     global_buffer
      - .actual_access:  read_only
        .address_space:  global
        .offset:         16
        .size:           8
        .value_kind:     global_buffer
      - .actual_access:  write_only
        .address_space:  global
        .offset:         24
        .size:           8
        .value_kind:     global_buffer
      - .offset:         32
        .size:           4
        .value_kind:     by_value
    .group_segment_fixed_size: 0
    .kernarg_segment_align: 8
    .kernarg_segment_size: 36
    .language:       OpenCL C
    .language_version:
      - 2
      - 0
    .max_flat_workgroup_size: 1024
    .name:           _Z14attn_bh_kernelPKDF16_S0_S0_PDF16_i
    .private_segment_fixed_size: 0
    .sgpr_count:     31
    .sgpr_spill_count: 0
    .symbol:         _Z14attn_bh_kernelPKDF16_S0_S0_PDF16_i.kd
    .uniform_work_group_size: 1
    .uses_dynamic_stack: false
    .vgpr_count:     120
    .vgpr_spill_count: 0
    .wavefront_size: 64
  - .agpr_count:     0
    .args:
      - .offset:         0
        .size:           336
        .value_kind:     by_value
    .group_segment_fixed_size: 0
    .kernarg_segment_align: 8
    .kernarg_segment_size: 336
    .language:       OpenCL C
    .language_version:
      - 2
      - 0
    .max_flat_workgroup_size: 256
    .name:           _Z11gemm_kernelILi0EEv8GemmArgs
    .private_segment_fixed_size: 0
    .sgpr_count:     47
    .sgpr_spill_count: 0
    .symbol:         _Z11gemm_kernelILi0EEv8GemmArgs.kd
    .uniform_work_group_size: 1
    .uses_dynamic_stack: false
    .vgpr_count:     198
    .vgpr_spill_count: 0
    .wavefront_size: 64
  - .agpr_count:     0
    .args:
      - .offset:         0
        .size:           336
        .value_kind:     by_value
    .group_segment_fixed_size: 0
    .kernarg_segment_align: 8
    .kernarg_segment_size: 336
    .language:       OpenCL C
    .language_version:
      - 2
      - 0
    .max_flat_workgroup_size: 256
    .name:           _Z11gemm_kernelILi1EEv8GemmArgs
    .private_segment_fixed_size: 0
    .sgpr_count:     43
    .sgpr_spill_count: 0
    .symbol:         _Z11gemm_kernelILi1EEv8GemmArgs.kd
    .uniform_work_group_size: 1
    .uses_dynamic_stack: false
    .vgpr_count:     202
    .vgpr_spill_count: 0
    .wavefront_size: 64
  - .agpr_count:     0
    .args:
      - .offset:         0
        .size:           336
        .value_kind:     by_value
    .group_segment_fixed_size: 0
    .kernarg_segment_align: 8
    .kernarg_segment_size: 336
    .language:       OpenCL C
    .language_version:
      - 2
      - 0
    .max_flat_workgroup_size: 256
    .name:           _Z11gemm_kernelILi2EEv8GemmArgs
    .private_segment_fixed_size: 0
    .sgpr_count:     41
    .sgpr_spill_count: 0
    .symbol:         _Z11gemm_kernelILi2EEv8GemmArgs.kd
    .uniform_work_group_size: 1
    .uses_dynamic_stack: false
    .vgpr_count:     198
    .vgpr_spill_count: 0
    .wavefront_size: 64
  - .agpr_count:     0
    .args:
      - .offset:         0
        .size:           336
        .value_kind:     by_value
      - .offset:         336
        .size:           4
        .value_kind:     hidden_block_count_x
      - .offset:         340
        .size:           4
        .value_kind:     hidden_block_count_y
      - .offset:         344
        .size:           4
        .value_kind:     hidden_block_count_z
      - .offset:         348
        .size:           2
        .value_kind:     hidden_group_size_x
      - .offset:         350
        .size:           2
        .value_kind:     hidden_group_size_y
      - .offset:         352
        .size:           2
        .value_kind:     hidden_group_size_z
      - .offset:         354
        .size:           2
        .value_kind:     hidden_remainder_x
      - .offset:         356
        .size:           2
        .value_kind:     hidden_remainder_y
      - .offset:         358
        .size:           2
        .value_kind:     hidden_remainder_z
      - .offset:         376
        .size:           8
        .value_kind:     hidden_global_offset_x
      - .offset:         384
        .size:           8
        .value_kind:     hidden_global_offset_y
      - .offset:         392
        .size:           8
        .value_kind:     hidden_global_offset_z
      - .offset:         400
        .size:           2
        .value_kind:     hidden_grid_dims
      - .offset:         456
        .size:           4
        .value_kind:     hidden_dynamic_lds_size
    .group_segment_fixed_size: 0
    .kernarg_segment_align: 8
    .kernarg_segment_size: 592
    .language:       OpenCL C
    .language_version:
      - 2
      - 0
    .max_flat_workgroup_size: 512
    .name:           _Z14gemm256_kernelILi0ELi512ELi1536EEv8GemmArgs
    .private_segment_fixed_size: 0
    .sgpr_count:     78
    .sgpr_spill_count: 0
    .symbol:         _Z14gemm256_kernelILi0ELi512ELi1536EEv8GemmArgs.kd
    .uniform_work_group_size: 1
    .uses_dynamic_stack: false
    .vgpr_count:     256
    .vgpr_spill_count: 0
    .wavefront_size: 64
  - .agpr_count:     0
    .args:
      - .offset:         0
        .size:           336
        .value_kind:     by_value
      - .offset:         336
        .size:           4
        .value_kind:     hidden_block_count_x
      - .offset:         340
        .size:           4
        .value_kind:     hidden_block_count_y
      - .offset:         344
        .size:           4
        .value_kind:     hidden_block_count_z
      - .offset:         348
        .size:           2
        .value_kind:     hidden_group_size_x
      - .offset:         350
        .size:           2
        .value_kind:     hidden_group_size_y
      - .offset:         352
        .size:           2
        .value_kind:     hidden_group_size_z
      - .offset:         354
        .size:           2
        .value_kind:     hidden_remainder_x
      - .offset:         356
        .size:           2
        .value_kind:     hidden_remainder_y
      - .offset:         358
        .size:           2
        .value_kind:     hidden_remainder_z
      - .offset:         376
        .size:           8
        .value_kind:     hidden_global_offset_x
      - .offset:         384
        .size:           8
        .value_kind:     hidden_global_offset_y
      - .offset:         392
        .size:           8
        .value_kind:     hidden_global_offset_z
      - .offset:         400
        .size:           2
        .value_kind:     hidden_grid_dims
      - .offset:         456
        .size:           4
        .value_kind:     hidden_dynamic_lds_size
    .group_segment_fixed_size: 0
    .kernarg_segment_align: 8
    .kernarg_segment_size: 592
    .language:       OpenCL C
    .language_version:
      - 2
      - 0
    .max_flat_workgroup_size: 512
    .name:           _Z14gemm256_kernelILi0ELi512ELi1024EEv8GemmArgs
    .private_segment_fixed_size: 0
    .sgpr_count:     78
    .sgpr_spill_count: 0
    .symbol:         _Z14gemm256_kernelILi0ELi512ELi1024EEv8GemmArgs.kd
    .uniform_work_group_size: 1
    .uses_dynamic_stack: false
    .vgpr_count:     256
    .vgpr_spill_count: 0
    .wavefront_size: 64
  - .agpr_count:     0
    .args:
      - .offset:         0
        .size:           336
        .value_kind:     by_value
      - .offset:         336
        .size:           4
        .value_kind:     hidden_block_count_x
      - .offset:         340
        .size:           4
        .value_kind:     hidden_block_count_y
      - .offset:         344
        .size:           4
        .value_kind:     hidden_block_count_z
      - .offset:         348
        .size:           2
        .value_kind:     hidden_group_size_x
      - .offset:         350
        .size:           2
        .value_kind:     hidden_group_size_y
      - .offset:         352
        .size:           2
        .value_kind:     hidden_group_size_z
      - .offset:         354
        .size:           2
        .value_kind:     hidden_remainder_x
      - .offset:         356
        .size:           2
        .value_kind:     hidden_remainder_y
      - .offset:         358
        .size:           2
        .value_kind:     hidden_remainder_z
      - .offset:         376
        .size:           8
        .value_kind:     hidden_global_offset_x
      - .offset:         384
        .size:           8
        .value_kind:     hidden_global_offset_y
      - .offset:         392
        .size:           8
        .value_kind:     hidden_global_offset_z
      - .offset:         400
        .size:           2
        .value_kind:     hidden_grid_dims
      - .offset:         456
        .size:           4
        .value_kind:     hidden_dynamic_lds_size
    .group_segment_fixed_size: 0
    .kernarg_segment_align: 8
    .kernarg_segment_size: 592
    .language:       OpenCL C
    .language_version:
      - 2
      - 0
    .max_flat_workgroup_size: 512
    .name:           _Z14gemm256_kernelILi1ELi512ELi512EEv8GemmArgs
    .private_segment_fixed_size: 0
    .sgpr_count:     81
    .sgpr_spill_count: 0
    .symbol:         _Z14gemm256_kernelILi1ELi512ELi512EEv8GemmArgs.kd
    .uniform_work_group_size: 1
    .uses_dynamic_stack: false
    .vgpr_count:     256
    .vgpr_spill_count: 0
    .wavefront_size: 64
  - .agpr_count:     0
    .args:
      - .offset:         0
        .size:           336
        .value_kind:     by_value
      - .offset:         336
        .size:           4
        .value_kind:     hidden_block_count_x
      - .offset:         340
        .size:           4
        .value_kind:     hidden_block_count_y
      - .offset:         344
        .size:           4
        .value_kind:     hidden_block_count_z
      - .offset:         348
        .size:           2
        .value_kind:     hidden_group_size_x
      - .offset:         350
        .size:           2
        .value_kind:     hidden_group_size_y
      - .offset:         352
        .size:           2
        .value_kind:     hidden_group_size_z
      - .offset:         354
        .size:           2
        .value_kind:     hidden_remainder_x
      - .offset:         356
        .size:           2
        .value_kind:     hidden_remainder_y
      - .offset:         358
        .size:           2
        .value_kind:     hidden_remainder_z
      - .offset:         376
        .size:           8
        .value_kind:     hidden_global_offset_x
      - .offset:         384
        .size:           8
        .value_kind:     hidden_global_offset_y
      - .offset:         392
        .size:           8
        .value_kind:     hidden_global_offset_z
      - .offset:         400
        .size:           2
        .value_kind:     hidden_grid_dims
      - .offset:         456
        .size:           4
        .value_kind:     hidden_dynamic_lds_size
    .group_segment_fixed_size: 0
    .kernarg_segment_align: 8
    .kernarg_segment_size: 592
    .language:       OpenCL C
    .language_version:
      - 2
      - 0
    .max_flat_workgroup_size: 512
    .name:           _Z14gemm256_kernelILi2ELi512ELi2048EEv8GemmArgs
    .private_segment_fixed_size: 0
    .sgpr_count:     68
    .sgpr_spill_count: 0
    .symbol:         _Z14gemm256_kernelILi2ELi512ELi2048EEv8GemmArgs.kd
    .uniform_work_group_size: 1
    .uses_dynamic_stack: false
    .vgpr_count:     254
    .vgpr_spill_count: 0
    .wavefront_size: 64
  - .agpr_count:     0
    .args:
      - .offset:         0
        .size:           336
        .value_kind:     by_value
      - .offset:         336
        .size:           4
        .value_kind:     hidden_block_count_x
      - .offset:         340
        .size:           4
        .value_kind:     hidden_block_count_y
      - .offset:         344
        .size:           4
        .value_kind:     hidden_block_count_z
      - .offset:         348
        .size:           2
        .value_kind:     hidden_group_size_x
      - .offset:         350
        .size:           2
        .value_kind:     hidden_group_size_y
      - .offset:         352
        .size:           2
        .value_kind:     hidden_group_size_z
      - .offset:         354
        .size:           2
        .value_kind:     hidden_remainder_x
      - .offset:         356
        .size:           2
        .value_kind:     hidden_remainder_y
      - .offset:         358
        .size:           2
        .value_kind:     hidden_remainder_z
      - .offset:         376
        .size:           8
        .value_kind:     hidden_global_offset_x
      - .offset:         384
        .size:           8
        .value_kind:     hidden_global_offset_y
      - .offset:         392
        .size:           8
        .value_kind:     hidden_global_offset_z
      - .offset:         400
        .size:           2
        .value_kind:     hidden_grid_dims
      - .offset:         456
        .size:           4
        .value_kind:     hidden_dynamic_lds_size
    .group_segment_fixed_size: 0
    .kernarg_segment_align: 8
    .kernarg_segment_size: 592
    .language:       OpenCL C
    .language_version:
      - 2
      - 0
    .max_flat_workgroup_size: 512
    .name:           _Z14gemm256_kernelILi1ELi2048ELi512EEv8GemmArgs
    .private_segment_fixed_size: 0
    .sgpr_count:     76
    .sgpr_spill_count: 0
    .symbol:         _Z14gemm256_kernelILi1ELi2048ELi512EEv8GemmArgs.kd
    .uniform_work_group_size: 1
    .uses_dynamic_stack: false
    .vgpr_count:     256
    .vgpr_spill_count: 0
    .wavefront_size: 64
  - .agpr_count:     0
    .args:
      - .offset:         0
        .size:           336
        .value_kind:     by_value
    .group_segment_fixed_size: 0
    .kernarg_segment_align: 8
    .kernarg_segment_size: 336
    .language:       OpenCL C
    .language_version:
      - 2
      - 0
    .max_flat_workgroup_size: 256
    .name:           _Z11gemm_kernelILi4EEv8GemmArgs
    .private_segment_fixed_size: 0
    .sgpr_count:     42
    .sgpr_spill_count: 0
    .symbol:         _Z11gemm_kernelILi4EEv8GemmArgs.kd
    .uniform_work_group_size: 1
    .uses_dynamic_stack: false
    .vgpr_count:     196
    .vgpr_spill_count: 0
    .wavefront_size: 64
  - .agpr_count:     0
    .args:
      - .offset:         0
        .size:           336
        .value_kind:     by_value
    .group_segment_fixed_size: 0
    .kernarg_segment_align: 8
    .kernarg_segment_size: 336
    .language:       OpenCL C
    .language_version:
      - 2
      - 0
    .max_flat_workgroup_size: 256
    .name:           _Z11gemm_kernelILi3EEv8GemmArgs
    .private_segment_fixed_size: 0
    .sgpr_count:     38
    .sgpr_spill_count: 0
    .symbol:         _Z11gemm_kernelILi3EEv8GemmArgs.kd
    .uniform_work_group_size: 1
    .uses_dynamic_stack: false
    .vgpr_count:     200
    .vgpr_spill_count: 0
    .wavefront_size: 64
